# v55 + router top-k: the three 8-lane argmax merge steps per round use DPP lane swizzles instead of two ds_bpermute round trips each (P1 and P5)
# speedup vs baseline: 1.0018x; 1.0018x over previous
.LBB0_135:
	s_or_b64 exec, exec, s[84:85]
	v_cndmask_b32_e64 v43, v43, v45, s[82:83]
	s_waitcnt lgkmcnt(0)
	v_cndmask_b32_e64 v44, v44, v46, s[82:83]
	s_nop 1
	v_mov_b32_dpp v45, v44 row_half_mirror row_mask:0xf bank_mask:0xf
	s_nop 1
	v_mov_b32_dpp v46, v43 row_half_mirror row_mask:0xf bank_mask:0xf
	s_waitcnt lgkmcnt(1)
	v_min_i32_e32 v47, v45, v44
	s_waitcnt lgkmcnt(0)
	v_cmp_eq_f32_e64 s[8:9], v43, v46
	s_nop 1
	v_cndmask_b32_e64 v44, v44, v47, s[8:9]
	v_cmp_lt_f32_e64 s[8:9], v43, v46
	s_nop 1
	v_cndmask_b32_e64 v43, v44, v45, s[8:9]
	v_ashrrev_i32_e32 v44, 5, v43
	v_lshlrev_b32_e64 v45, v43, 1
	v_cmp_eq_u32_e64 s[8:9], v44, v10
	s_nop 1
	v_cndmask_b32_e64 v44, 0, v45, s[8:9]
	v_cmp_eq_u32_e64 s[8:9], s29, v10
	s_add_i32 s29, s29, 1
	v_or_b32_e32 v39, v44, v39
	s_cmp_lg_u32 s29, 8
	v_cndmask_b32_e64 v2, v2, v43, s[8:9]
	s_cbranch_scc0 .LBB0_87
.LBB0_136:
	v_and_b32_e32 v43, 1, v39
	v_cmp_eq_u32_e64 s[8:9], 1, v43
	s_or_b64 s[8:9], s[4:5], s[8:9]
	v_and_b32_e32 v44, 2, v39
	v_cndmask_b32_e64 v43, v14, v220, s[8:9]
	v_cmp_eq_u32_e64 s[8:9], 0, v44
	v_cmp_gt_f32_e64 s[10:11], v15, v43
	s_and_b64 s[8:9], s[8:9], s[10:11]
	v_cndmask_b32_e64 v43, v43, v15, s[8:9]
	v_and_b32_e32 v45, 4, v39
	v_cndmask_b32_e64 v44, 0, 1, s[8:9]
	v_cmp_eq_u32_e64 s[8:9], 0, v45
	v_cmp_gt_f32_e64 s[10:11], v16, v43
	s_and_b64 s[8:9], s[8:9], s[10:11]
	v_cndmask_b32_e64 v43, v43, v16, s[8:9]
	v_and_b32_e32 v45, 8, v39
	v_cndmask_b32_e64 v44, v44, 2, s[8:9]
	v_cmp_eq_u32_e64 s[8:9], 0, v45
	v_cmp_gt_f32_e64 s[10:11], v17, v43
	s_and_b64 s[8:9], s[8:9], s[10:11]
	v_cndmask_b32_e64 v43, v43, v17, s[8:9]
	v_and_b32_e32 v45, 16, v39
	v_cndmask_b32_e64 v44, v44, 3, s[8:9]
	v_cmp_eq_u32_e64 s[8:9], 0, v45
	v_cmp_gt_f32_e64 s[10:11], v18, v43
	s_and_b64 s[8:9], s[8:9], s[10:11]
	v_cndmask_b32_e64 v43, v43, v18, s[8:9]
	v_and_b32_e32 v45, 32, v39
	v_cndmask_b32_e64 v44, v44, 4, s[8:9]
	v_cmp_eq_u32_e64 s[8:9], 0, v45
	v_cmp_gt_f32_e64 s[10:11], v19, v43
	s_and_b64 s[8:9], s[8:9], s[10:11]
	v_cndmask_b32_e64 v43, v43, v19, s[8:9]
	v_and_b32_e32 v45, 64, v39
	v_cndmask_b32_e64 v44, v44, 5, s[8:9]
	v_cmp_eq_u32_e64 s[8:9], 0, v45
	v_cmp_gt_f32_e64 s[10:11], v20, v43
	s_and_b64 s[8:9], s[8:9], s[10:11]
	v_cndmask_b32_e64 v43, v43, v20, s[8:9]
	v_and_b32_e32 v45, 0x80, v39
	v_cndmask_b32_e64 v44, v44, 6, s[8:9]
	v_cmp_eq_u32_e64 s[8:9], 0, v45
	v_cmp_gt_f32_e64 s[10:11], v21, v43
	s_and_b64 s[8:9], s[8:9], s[10:11]
	v_cndmask_b32_e64 v43, v43, v21, s[8:9]
	v_and_b32_e32 v45, 0x100, v39
	v_cndmask_b32_e64 v44, v44, 7, s[8:9]
	v_cmp_eq_u32_e64 s[8:9], 0, v45
	v_cmp_gt_f32_e64 s[10:11], v22, v43
	s_and_b64 s[8:9], s[8:9], s[10:11]
	v_cndmask_b32_e64 v43, v43, v22, s[8:9]
	v_and_b32_e32 v45, 0x200, v39
	v_cndmask_b32_e64 v44, v44, 8, s[8:9]
	v_cmp_eq_u32_e64 s[8:9], 0, v45
	v_cmp_gt_f32_e64 s[10:11], v23, v43
	s_and_b64 s[8:9], s[8:9], s[10:11]
	v_cndmask_b32_e64 v43, v43, v23, s[8:9]
	v_and_b32_e32 v45, 0x400, v39
	v_cndmask_b32_e64 v44, v44, 9, s[8:9]
	v_cmp_eq_u32_e64 s[8:9], 0, v45
	v_cmp_gt_f32_e64 s[10:11], v24, v43
	s_and_b64 s[8:9], s[8:9], s[10:11]
	v_cndmask_b32_e64 v43, v43, v24, s[8:9]
	v_and_b32_e32 v45, 0x800, v39
	v_cndmask_b32_e64 v44, v44, 10, s[8:9]
	v_cmp_eq_u32_e64 s[8:9], 0, v45
	v_cmp_gt_f32_e64 s[10:11], v25, v43
	s_and_b64 s[8:9], s[8:9], s[10:11]
	v_cndmask_b32_e64 v43, v43, v25, s[8:9]
	v_and_b32_e32 v45, 0x1000, v39
	v_cndmask_b32_e64 v44, v44, 11, s[8:9]
	v_cmp_eq_u32_e64 s[8:9], 0, v45
	v_cmp_gt_f32_e64 s[10:11], v26, v43
	s_and_b64 s[8:9], s[8:9], s[10:11]
	v_cndmask_b32_e64 v43, v43, v26, s[8:9]
	v_and_b32_e32 v45, 0x2000, v39
	v_cndmask_b32_e64 v44, v44, 12, s[8:9]
	v_cmp_eq_u32_e64 s[8:9], 0, v45
	v_cmp_gt_f32_e64 s[10:11], v27, v43
	s_and_b64 s[8:9], s[8:9], s[10:11]
	v_cndmask_b32_e64 v43, v43, v27, s[8:9]
	v_and_b32_e32 v45, 0x4000, v39
	v_cndmask_b32_e64 v44, v44, 13, s[8:9]
	v_cmp_eq_u32_e64 s[8:9], 0, v45
	v_cmp_gt_f32_e64 s[10:11], v28, v43
	s_and_b64 s[8:9], s[8:9], s[10:11]
	v_cndmask_b32_e64 v43, v43, v28, s[8:9]
	v_and_b32_e32 v45, 0x8000, v39
	v_cndmask_b32_e64 v44, v44, 14, s[8:9]
	v_cmp_eq_u32_e64 s[8:9], 0, v45
	v_cmp_gt_f32_e64 s[10:11], v29, v43
	s_and_b64 s[8:9], s[8:9], s[10:11]
	v_cndmask_b32_e64 v43, v43, v29, s[8:9]
	v_and_b32_e32 v45, 0x10000, v39
	v_cndmask_b32_e64 v44, v44, 15, s[8:9]
	v_cmp_eq_u32_e64 s[8:9], 0, v45
	v_cmp_gt_f32_e64 s[10:11], v30, v43
	s_and_b64 s[8:9], s[8:9], s[10:11]
	v_cndmask_b32_e64 v43, v43, v30, s[8:9]
	v_and_b32_e32 v45, 0x20000, v39
	v_cndmask_b32_e64 v44, v44, 16, s[8:9]
	v_cmp_eq_u32_e64 s[8:9], 0, v45
	v_cmp_gt_f32_e64 s[10:11], v31, v43
	s_and_b64 s[8:9], s[8:9], s[10:11]
	v_cndmask_b32_e64 v43, v43, v31, s[8:9]
	v_and_b32_e32 v45, 0x40000, v39
	v_cndmask_b32_e64 v44, v44, 17, s[8:9]
	v_cmp_eq_u32_e64 s[8:9], 0, v45
	v_cmp_gt_f32_e64 s[10:11], v32, v43
	s_and_b64 s[8:9], s[8:9], s[10:11]
	v_cndmask_b32_e64 v43, v43, v32, s[8:9]
	v_and_b32_e32 v45, 0x80000, v39
	v_cndmask_b32_e64 v44, v44, 18, s[8:9]
	v_cmp_eq_u32_e64 s[8:9], 0, v45
	v_cmp_gt_f32_e64 s[10:11], v33, v43
	s_and_b64 s[8:9], s[8:9], s[10:11]
	v_cndmask_b32_e64 v43, v43, v33, s[8:9]
	v_and_b32_e32 v45, 0x100000, v39
	v_cndmask_b32_e64 v44, v44, 19, s[8:9]
	v_cmp_eq_u32_e64 s[8:9], 0, v45
	v_cmp_gt_f32_e64 s[10:11], v34, v43
	s_and_b64 s[8:9], s[8:9], s[10:11]
	v_cndmask_b32_e64 v43, v43, v34, s[8:9]
	v_and_b32_e32 v45, 0x200000, v39
	v_cndmask_b32_e64 v44, v44, 20, s[8:9]
	v_cmp_eq_u32_e64 s[8:9], 0, v45
	v_cmp_gt_f32_e64 s[10:11], v35, v43
	s_and_b64 s[8:9], s[8:9], s[10:11]
	v_cndmask_b32_e64 v43, v43, v35, s[8:9]
	v_and_b32_e32 v45, 0x400000, v39
	v_cndmask_b32_e64 v44, v44, 21, s[8:9]
	v_cmp_eq_u32_e64 s[8:9], 0, v45
	v_cmp_gt_f32_e64 s[10:11], v36, v43
	s_and_b64 s[8:9], s[8:9], s[10:11]
	v_cndmask_b32_e64 v43, v43, v36, s[8:9]
	v_and_b32_e32 v45, 0x800000, v39
	v_cndmask_b32_e64 v44, v44, 22, s[8:9]
	v_cmp_eq_u32_e64 s[8:9], 0, v45
	v_cmp_gt_f32_e64 s[10:11], v37, v43
	s_and_b64 s[8:9], s[8:9], s[10:11]
	v_cndmask_b32_e64 v43, v43, v37, s[8:9]
	v_and_b32_e32 v45, 0x1000000, v39
	v_cndmask_b32_e64 v44, v44, 23, s[8:9]
	v_cmp_eq_u32_e64 s[8:9], 0, v45
	v_cmp_gt_f32_e64 s[10:11], v6, v43
	s_and_b64 s[8:9], s[8:9], s[10:11]
	v_cndmask_b32_e64 v43, v43, v6, s[8:9]
	v_and_b32_e32 v45, 0x2000000, v39
	v_cndmask_b32_e64 v44, v44, 24, s[8:9]
	v_cmp_eq_u32_e64 s[8:9], 0, v45
	v_cmp_gt_f32_e64 s[10:11], v7, v43
	s_and_b64 s[8:9], s[8:9], s[10:11]
	v_cndmask_b32_e64 v43, v43, v7, s[8:9]
	v_and_b32_e32 v45, 0x4000000, v39
	v_cndmask_b32_e64 v44, v44, 25, s[8:9]
	v_cmp_eq_u32_e64 s[8:9], 0, v45
	v_cmp_gt_f32_e64 s[10:11], v8, v43
	s_and_b64 s[8:9], s[8:9], s[10:11]
	v_cndmask_b32_e64 v43, v43, v8, s[8:9]
	v_and_b32_e32 v45, 0x8000000, v39
	v_cndmask_b32_e64 v44, v44, 26, s[8:9]
	v_cmp_eq_u32_e64 s[8:9], 0, v45
	v_cmp_gt_f32_e64 s[10:11], v9, v43
	s_and_b64 s[8:9], s[8:9], s[10:11]
	v_cndmask_b32_e64 v43, v43, v9, s[8:9]
	v_and_b32_e32 v45, 0x10000000, v39
	v_cndmask_b32_e64 v44, v44, 27, s[8:9]
	v_cmp_eq_u32_e64 s[8:9], 0, v45
	v_cmp_gt_f32_e64 s[10:11], v38, v43
	s_and_b64 s[8:9], s[8:9], s[10:11]
	v_cndmask_b32_e64 v43, v43, v38, s[8:9]
	v_and_b32_e32 v45, 0x20000000, v39
	v_cndmask_b32_e64 v44, v44, 28, s[8:9]
	v_cmp_eq_u32_e64 s[8:9], 0, v45
	v_cmp_gt_f32_e64 s[10:11], v3, v43
	s_and_b64 s[8:9], s[8:9], s[10:11]
	v_cndmask_b32_e64 v43, v43, v3, s[8:9]
	v_and_b32_e32 v45, 2.0, v39
	v_cndmask_b32_e64 v44, v44, 29, s[8:9]
	v_cmp_eq_u32_e64 s[8:9], 0, v45
	v_cmp_gt_f32_e64 s[10:11], v4, v43
	s_and_b64 s[8:9], s[8:9], s[10:11]
	v_cndmask_b32_e64 v43, v43, v4, s[8:9]
	v_cndmask_b32_e64 v44, v44, 30, s[8:9]
	v_cmp_lt_i32_e64 s[8:9], -1, v39
	v_cmp_gt_f32_e64 s[10:11], v5, v43
	s_and_b64 s[8:9], s[8:9], s[10:11]
	v_cndmask_b32_e64 v43, v43, v5, s[8:9]
	v_cndmask_b32_e64 v45, v44, 31, s[8:9]
	v_cndmask_b32_e32 v43, v220, v43, vcc
	s_nop 1
	v_mov_b32_dpp v44, v43 quad_perm:[1,0,3,2] row_mask:0xf bank_mask:0xf
	v_or_b32_e32 v45, v45, v13
	s_nop 1
	v_mov_b32_dpp v46, v45 quad_perm:[1,0,3,2] row_mask:0xf bank_mask:0xf
	s_mov_b64 s[82:83], -1
	s_mov_b64 s[10:11], -1
	s_waitcnt lgkmcnt(1)
	v_cmp_nlt_f32_e64 s[8:9], v43, v44
	s_and_saveexec_b64 s[84:85], s[8:9]
	s_cbranch_execz .LBB0_138
	v_cmp_eq_f32_e64 s[8:9], v43, v44
	s_waitcnt lgkmcnt(0)
	v_cmp_lt_i32_e64 s[10:11], v46, v45
	s_and_b64 s[8:9], s[8:9], s[10:11]
	s_orn2_b64 s[10:11], s[8:9], exec
.LBB0_138:
	s_or_b64 exec, exec, s[84:85]
	v_cndmask_b32_e64 v43, v43, v44, s[10:11]
	s_waitcnt lgkmcnt(0)
	v_cndmask_b32_e64 v44, v45, v46, s[10:11]
	s_nop 1
	v_mov_b32_dpp v45, v43 quad_perm:[2,3,0,1] row_mask:0xf bank_mask:0xf
	s_nop 1
	v_mov_b32_dpp v46, v44 quad_perm:[2,3,0,1] row_mask:0xf bank_mask:0xf
	s_waitcnt lgkmcnt(1)
	v_cmp_nlt_f32_e64 s[8:9], v43, v45
	s_and_saveexec_b64 s[84:85], s[8:9]
	s_cbranch_execz .LBB0_135
	v_cmp_eq_f32_e64 s[8:9], v43, v45
	s_waitcnt lgkmcnt(0)
	v_cmp_lt_i32_e64 s[10:11], v46, v44
	s_and_b64 s[8:9], s[8:9], s[10:11]
	s_orn2_b64 s[82:83], s[8:9], exec
	s_branch .LBB0_135

.LBB0_771:
	s_or_b64 exec, exec, s[76:77]
	v_cndmask_b32_e64 v43, v43, v45, s[74:75]
	s_waitcnt lgkmcnt(0)
	v_cndmask_b32_e64 v44, v44, v46, s[74:75]
	s_nop 1
	v_mov_b32_dpp v45, v44 row_half_mirror row_mask:0xf bank_mask:0xf
	s_nop 1
	v_mov_b32_dpp v46, v43 row_half_mirror row_mask:0xf bank_mask:0xf
	s_waitcnt lgkmcnt(1)
	v_min_i32_e32 v47, v45, v44
	s_waitcnt lgkmcnt(0)
	v_cmp_eq_f32_e64 s[12:13], v43, v46
	s_nop 1
	v_cndmask_b32_e64 v44, v44, v47, s[12:13]
	v_cmp_lt_f32_e64 s[12:13], v43, v46
	s_nop 1
	v_cndmask_b32_e64 v43, v44, v45, s[12:13]
	v_ashrrev_i32_e32 v44, 5, v43
	v_lshlrev_b32_e64 v45, v43, 1
	v_cmp_eq_u32_e64 s[12:13], v44, v4
	s_nop 1
	v_cndmask_b32_e64 v44, 0, v45, s[12:13]
	v_cmp_eq_u32_e64 s[12:13], s31, v4
	s_add_i32 s31, s31, 1
	v_or_b32_e32 v39, v44, v39
	s_cmp_lg_u32 s31, 8
	v_cndmask_b32_e64 v2, v2, v43, s[12:13]
	s_cbranch_scc0 .LBB0_753
.LBB0_772:
	v_and_b32_e32 v43, 1, v39
	v_cmp_eq_u32_e64 s[12:13], 1, v43
	s_or_b64 s[12:13], s[10:11], s[12:13]
	v_and_b32_e32 v44, 2, v39
	v_cndmask_b32_e64 v43, v6, v219, s[12:13]
	v_cmp_eq_u32_e64 s[12:13], 0, v44
	v_cmp_gt_f32_e64 s[14:15], v7, v43
	s_and_b64 s[12:13], s[12:13], s[14:15]
	v_cndmask_b32_e64 v43, v43, v7, s[12:13]
	v_and_b32_e32 v45, 4, v39
	v_cndmask_b32_e64 v44, 0, 1, s[12:13]
	v_cmp_eq_u32_e64 s[12:13], 0, v45
	v_cmp_gt_f32_e64 s[14:15], v8, v43
	s_and_b64 s[12:13], s[12:13], s[14:15]
	v_cndmask_b32_e64 v43, v43, v8, s[12:13]
	v_and_b32_e32 v45, 8, v39
	v_cndmask_b32_e64 v44, v44, 2, s[12:13]
	v_cmp_eq_u32_e64 s[12:13], 0, v45
	v_cmp_gt_f32_e64 s[14:15], v9, v43
	s_and_b64 s[12:13], s[12:13], s[14:15]
	v_cndmask_b32_e64 v43, v43, v9, s[12:13]
	v_and_b32_e32 v45, 16, v39
	v_cndmask_b32_e64 v44, v44, 3, s[12:13]
	v_cmp_eq_u32_e64 s[12:13], 0, v45
	v_cmp_gt_f32_e64 s[14:15], v10, v43
	s_and_b64 s[12:13], s[12:13], s[14:15]
	v_cndmask_b32_e64 v43, v43, v10, s[12:13]
	v_and_b32_e32 v45, 32, v39
	v_cndmask_b32_e64 v44, v44, 4, s[12:13]
	v_cmp_eq_u32_e64 s[12:13], 0, v45
	v_cmp_gt_f32_e64 s[14:15], v11, v43
	s_and_b64 s[12:13], s[12:13], s[14:15]
	v_cndmask_b32_e64 v43, v43, v11, s[12:13]
	v_and_b32_e32 v45, 64, v39
	v_cndmask_b32_e64 v44, v44, 5, s[12:13]
	v_cmp_eq_u32_e64 s[12:13], 0, v45
	v_cmp_gt_f32_e64 s[14:15], v12, v43
	s_and_b64 s[12:13], s[12:13], s[14:15]
	v_cndmask_b32_e64 v43, v43, v12, s[12:13]
	v_and_b32_e32 v45, 0x80, v39
	v_cndmask_b32_e64 v44, v44, 6, s[12:13]
	v_cmp_eq_u32_e64 s[12:13], 0, v45
	v_cmp_gt_f32_e64 s[14:15], v13, v43
	s_and_b64 s[12:13], s[12:13], s[14:15]
	v_cndmask_b32_e64 v43, v43, v13, s[12:13]
	v_and_b32_e32 v45, 0x100, v39
	v_cndmask_b32_e64 v44, v44, 7, s[12:13]
	v_cmp_eq_u32_e64 s[12:13], 0, v45
	v_cmp_gt_f32_e64 s[14:15], v14, v43
	s_and_b64 s[12:13], s[12:13], s[14:15]
	v_cndmask_b32_e64 v43, v43, v14, s[12:13]
	v_and_b32_e32 v45, 0x200, v39
	v_cndmask_b32_e64 v44, v44, 8, s[12:13]
	v_cmp_eq_u32_e64 s[12:13], 0, v45
	v_cmp_gt_f32_e64 s[14:15], v15, v43
	s_and_b64 s[12:13], s[12:13], s[14:15]
	v_cndmask_b32_e64 v43, v43, v15, s[12:13]
	v_and_b32_e32 v45, 0x400, v39
	v_cndmask_b32_e64 v44, v44, 9, s[12:13]
	v_cmp_eq_u32_e64 s[12:13], 0, v45
	v_cmp_gt_f32_e64 s[14:15], v16, v43
	s_and_b64 s[12:13], s[12:13], s[14:15]
	v_cndmask_b32_e64 v43, v43, v16, s[12:13]
	v_and_b32_e32 v45, 0x800, v39
	v_cndmask_b32_e64 v44, v44, 10, s[12:13]
	v_cmp_eq_u32_e64 s[12:13], 0, v45
	v_cmp_gt_f32_e64 s[14:15], v17, v43
	s_and_b64 s[12:13], s[12:13], s[14:15]
	v_cndmask_b32_e64 v43, v43, v17, s[12:13]
	v_and_b32_e32 v45, 0x1000, v39
	v_cndmask_b32_e64 v44, v44, 11, s[12:13]
	v_cmp_eq_u32_e64 s[12:13], 0, v45
	v_cmp_gt_f32_e64 s[14:15], v18, v43
	s_and_b64 s[12:13], s[12:13], s[14:15]
	v_cndmask_b32_e64 v43, v43, v18, s[12:13]
	v_and_b32_e32 v45, 0x2000, v39
	v_cndmask_b32_e64 v44, v44, 12, s[12:13]
	v_cmp_eq_u32_e64 s[12:13], 0, v45
	v_cmp_gt_f32_e64 s[14:15], v19, v43
	s_and_b64 s[12:13], s[12:13], s[14:15]
	v_cndmask_b32_e64 v43, v43, v19, s[12:13]
	v_and_b32_e32 v45, 0x4000, v39
	v_cndmask_b32_e64 v44, v44, 13, s[12:13]
	v_cmp_eq_u32_e64 s[12:13], 0, v45
	v_cmp_gt_f32_e64 s[14:15], v20, v43
	s_and_b64 s[12:13], s[12:13], s[14:15]
	v_cndmask_b32_e64 v43, v43, v20, s[12:13]
	v_and_b32_e32 v45, 0x8000, v39
	v_cndmask_b32_e64 v44, v44, 14, s[12:13]
	v_cmp_eq_u32_e64 s[12:13], 0, v45
	v_cmp_gt_f32_e64 s[14:15], v21, v43
	s_and_b64 s[12:13], s[12:13], s[14:15]
	v_cndmask_b32_e64 v43, v43, v21, s[12:13]
	v_and_b32_e32 v45, 0x10000, v39
	v_cndmask_b32_e64 v44, v44, 15, s[12:13]
	v_cmp_eq_u32_e64 s[12:13], 0, v45
	v_cmp_gt_f32_e64 s[14:15], v22, v43
	s_and_b64 s[12:13], s[12:13], s[14:15]
	v_cndmask_b32_e64 v43, v43, v22, s[12:13]
	v_and_b32_e32 v45, 0x20000, v39
	v_cndmask_b32_e64 v44, v44, 16, s[12:13]
	v_cmp_eq_u32_e64 s[12:13], 0, v45
	v_cmp_gt_f32_e64 s[14:15], v23, v43
	s_and_b64 s[12:13], s[12:13], s[14:15]
	v_cndmask_b32_e64 v43, v43, v23, s[12:13]
	v_and_b32_e32 v45, 0x40000, v39
	v_cndmask_b32_e64 v44, v44, 17, s[12:13]
	v_cmp_eq_u32_e64 s[12:13], 0, v45
	v_cmp_gt_f32_e64 s[14:15], v24, v43
	s_and_b64 s[12:13], s[12:13], s[14:15]
	v_cndmask_b32_e64 v43, v43, v24, s[12:13]
	v_and_b32_e32 v45, 0x80000, v39
	v_cndmask_b32_e64 v44, v44, 18, s[12:13]
	v_cmp_eq_u32_e64 s[12:13], 0, v45
	v_cmp_gt_f32_e64 s[14:15], v25, v43
	s_and_b64 s[12:13], s[12:13], s[14:15]
	v_cndmask_b32_e64 v43, v43, v25, s[12:13]
	v_and_b32_e32 v45, 0x100000, v39
	v_cndmask_b32_e64 v44, v44, 19, s[12:13]
	v_cmp_eq_u32_e64 s[12:13], 0, v45
	v_cmp_gt_f32_e64 s[14:15], v26, v43
	s_and_b64 s[12:13], s[12:13], s[14:15]
	v_cndmask_b32_e64 v43, v43, v26, s[12:13]
	v_and_b32_e32 v45, 0x200000, v39
	v_cndmask_b32_e64 v44, v44, 20, s[12:13]
	v_cmp_eq_u32_e64 s[12:13], 0, v45
	v_cmp_gt_f32_e64 s[14:15], v27, v43
	s_and_b64 s[12:13], s[12:13], s[14:15]
	v_cndmask_b32_e64 v43, v43, v27, s[12:13]
	v_and_b32_e32 v45, 0x400000, v39
	v_cndmask_b32_e64 v44, v44, 21, s[12:13]
	v_cmp_eq_u32_e64 s[12:13], 0, v45
	v_cmp_gt_f32_e64 s[14:15], v28, v43
	s_and_b64 s[12:13], s[12:13], s[14:15]
	v_cndmask_b32_e64 v43, v43, v28, s[12:13]
	v_and_b32_e32 v45, 0x800000, v39
	v_cndmask_b32_e64 v44, v44, 22, s[12:13]
	v_cmp_eq_u32_e64 s[12:13], 0, v45
	v_cmp_gt_f32_e64 s[14:15], v29, v43
	s_and_b64 s[12:13], s[12:13], s[14:15]
	v_cndmask_b32_e64 v43, v43, v29, s[12:13]
	v_and_b32_e32 v45, 0x1000000, v39
	v_cndmask_b32_e64 v44, v44, 23, s[12:13]
	v_cmp_eq_u32_e64 s[12:13], 0, v45
	v_cmp_gt_f32_e64 s[14:15], v30, v43
	s_and_b64 s[12:13], s[12:13], s[14:15]
	v_cndmask_b32_e64 v43, v43, v30, s[12:13]
	v_and_b32_e32 v45, 0x2000000, v39
	v_cndmask_b32_e64 v44, v44, 24, s[12:13]
	v_cmp_eq_u32_e64 s[12:13], 0, v45
	v_cmp_gt_f32_e64 s[14:15], v31, v43
	s_and_b64 s[12:13], s[12:13], s[14:15]
	v_cndmask_b32_e64 v43, v43, v31, s[12:13]
	v_and_b32_e32 v45, 0x4000000, v39
	v_cndmask_b32_e64 v44, v44, 25, s[12:13]
	v_cmp_eq_u32_e64 s[12:13], 0, v45
	v_cmp_gt_f32_e64 s[14:15], v32, v43
	s_and_b64 s[12:13], s[12:13], s[14:15]
	v_cndmask_b32_e64 v43, v43, v32, s[12:13]
	v_and_b32_e32 v45, 0x8000000, v39
	v_cndmask_b32_e64 v44, v44, 26, s[12:13]
	v_cmp_eq_u32_e64 s[12:13], 0, v45
	v_cmp_gt_f32_e64 s[14:15], v33, v43
	s_and_b64 s[12:13], s[12:13], s[14:15]
	v_cndmask_b32_e64 v43, v43, v33, s[12:13]
	v_and_b32_e32 v45, 0x10000000, v39
	v_cndmask_b32_e64 v44, v44, 27, s[12:13]
	v_cmp_eq_u32_e64 s[12:13], 0, v45
	v_cmp_gt_f32_e64 s[14:15], v34, v43
	s_and_b64 s[12:13], s[12:13], s[14:15]
	v_cndmask_b32_e64 v43, v43, v34, s[12:13]
	v_and_b32_e32 v45, 0x20000000, v39
	v_cndmask_b32_e64 v44, v44, 28, s[12:13]
	v_cmp_eq_u32_e64 s[12:13], 0, v45
	v_cmp_gt_f32_e64 s[14:15], v35, v43
	s_and_b64 s[12:13], s[12:13], s[14:15]
	v_cndmask_b32_e64 v43, v43, v35, s[12:13]
	v_and_b32_e32 v45, 2.0, v39
	v_cndmask_b32_e64 v44, v44, 29, s[12:13]
	v_cmp_eq_u32_e64 s[12:13], 0, v45
	v_cmp_gt_f32_e64 s[14:15], v36, v43
	s_and_b64 s[12:13], s[12:13], s[14:15]
	v_cndmask_b32_e64 v43, v43, v36, s[12:13]
	v_cndmask_b32_e64 v44, v44, 30, s[12:13]
	v_cmp_lt_i32_e64 s[12:13], -1, v39
	v_cmp_gt_f32_e64 s[14:15], v37, v43
	s_and_b64 s[12:13], s[12:13], s[14:15]
	v_cndmask_b32_e64 v43, v43, v37, s[12:13]
	v_cndmask_b32_e64 v44, v44, 31, s[12:13]
	v_cndmask_b32_e32 v43, v219, v43, vcc
	s_nop 1
	v_mov_b32_dpp v45, v43 quad_perm:[1,0,3,2] row_mask:0xf bank_mask:0xf
	v_or_b32_e32 v44, v44, v38
	s_nop 1
	v_mov_b32_dpp v46, v44 quad_perm:[1,0,3,2] row_mask:0xf bank_mask:0xf
	s_mov_b64 s[74:75], -1
	s_mov_b64 s[14:15], -1
	s_waitcnt lgkmcnt(1)
	v_cmp_nlt_f32_e64 s[12:13], v43, v45
	s_and_saveexec_b64 s[76:77], s[12:13]
	s_cbranch_execz .LBB0_774
	v_cmp_eq_f32_e64 s[12:13], v43, v45
	s_waitcnt lgkmcnt(0)
	v_cmp_lt_i32_e64 s[14:15], v46, v44
	s_and_b64 s[12:13], s[12:13], s[14:15]
	s_orn2_b64 s[14:15], s[12:13], exec
.LBB0_774:
	s_or_b64 exec, exec, s[76:77]
	v_cndmask_b32_e64 v43, v43, v45, s[14:15]
	s_waitcnt lgkmcnt(0)
	v_cndmask_b32_e64 v44, v44, v46, s[14:15]
	s_nop 1
	v_mov_b32_dpp v45, v43 quad_perm:[2,3,0,1] row_mask:0xf bank_mask:0xf
	s_nop 1
	v_mov_b32_dpp v46, v44 quad_perm:[2,3,0,1] row_mask:0xf bank_mask:0xf
	s_waitcnt lgkmcnt(1)
	v_cmp_nlt_f32_e64 s[12:13], v43, v45
	s_and_saveexec_b64 s[76:77], s[12:13]
	s_cbranch_execz .LBB0_771
	v_cmp_eq_f32_e64 s[12:13], v43, v45
	s_waitcnt lgkmcnt(0)
	v_cmp_lt_i32_e64 s[14:15], v46, v44
	s_and_b64 s[12:13], s[12:13], s[14:15]
	s_orn2_b64 s[74:75], s[12:13], exec
	s_branch .LBB0_771
